# n18_early2_cap
# baseline (speedup 1.0000x reference)
.Lrec_own_retry:
	s_cmp_lg_u32 s47, 0
	s_cbranch_scc1 .Lrec_own_ok
	s_add_i32 s44, s44, 1
	s_cmp_gt_u32 s44, 0x61a80
	s_cbranch_scc1 .Lrec_own_die
	global_load_lds_dwordx4 v176, s[40:41] sc1
	global_load_lds_dwordx4 v176, s[40:41] offset:1024 sc1
	global_load_lds_dwordx4 v176, s[40:41] offset:2048 sc1
	global_load_lds_dwordx4 v176, s[40:41] offset:3072 sc1
	s_waitcnt vmcnt(0)
	ds_read_b128 v[138:141], v166
	ds_read_b128 v[142:145], v166 offset:1024
	ds_read_b128 v[146:149], v166 offset:2048
	ds_read_b128 v[150:153], v166 offset:3072
	s_branch .Lrec_own_mf
